# weight-converter drain loops of P1 tail, P4 and P9: counted vmcnt waits keep the next load batch in flight during conversion
# speedup vs baseline: 1.0035x; 1.0035x over previous
;     __device__ __forceinline__ CvtDesc desc(int qq) const { return cvt_desc(*F, item_of(qq), qq & 1, h); }
;     __device__ __forceinline__ void proc() { cvt_to_lds(buf, desc(q), img, gl, q & 1, h, F->lane); if (q & 1) fitem = item_of(q); ++q; }
;     __device__ __forceinline__ void flush() { if (fitem >= 0) { cvt_flush(cvt_desc(*F, fitem, 0, h), img, h, F->lane); fitem = -1; } }
;     __device__ __forceinline__ void drain() {
;         __syncthreads(); flush(); __syncthreads();
;         if (state != 0) { proc(); state = 0; if (fitem >= 0) { __syncthreads(); flush(); __syncthreads(); } }
;         if (q >= nq) { __syncthreads(); return; }
;         CvtBuf b2;
;         cvt_load(buf, desc(q), F->lane);
;         while (q < nq) {
;             if (q + 1 < nq) cvt_load(b2, desc(q + 1), F->lane);
;             cvt_to_lds(buf, desc(q), img, gl, q & 1, h, F->lane); if (q & 1) fitem = item_of(q); ++q;
;             if (fitem >= 0) { __syncthreads(); flush(); __syncthreads(); }
;             if (q >= nq) break;
;             if (q + 1 < nq) cvt_load(buf, desc(q + 1), F->lane);
;             cvt_to_lds(b2, desc(q), img, gl, q & 1, h, F->lane); if (q & 1) fitem = item_of(q); ++q;
.LBB0_294:
	s_or_b32 s0, s43, 1
	s_cmp_lt_i32 s0, s34
	s_cselect_b64 s[6:7], -1, 0
	s_lshr_b32 s1, s43, 1
	s_mul_i32 s44, s1, 0xc0
	s_add_i32 s44, s44, s3
	s_cmp_ge_i32 s0, s34
	s_cbranch_scc0 .Ldr1_goA
	s_waitcnt vmcnt(0)
	s_branch .LBB0_300
.Ldr1_goA:
	s_cmpk_gt_i32 s44, 0x3fff
	s_mov_b64 s[14:15], -1
	s_cbranch_scc0 .LBB0_297
	s_add_i32 s0, s44, 0xffffc000
	s_lshr_b32 s4, s0, 8
	v_readlane_b32 s8, v254, 0
	s_lshr_b32 s36, s44, 4
	s_lshl_b64 s[0:1], s[4:5], 24
	v_readlane_b32 s10, v254, 2
	v_readlane_b32 s11, v254, 3
	v_readlane_b32 s14, v254, 6
	v_readlane_b32 s15, v254, 7
	s_add_u32 s0, s10, s0
	v_readlane_b32 s9, v254, 1
	v_readlane_b32 s12, v254, 4
	v_readlane_b32 s13, v254, 5
	s_addc_u32 s1, s11, s1
	s_mov_b64 s[14:15], 0

; #define LAS __attribute__((address_space(3)))
; __device__ __forceinline__ unsigned pk4_fp8(float a, float b, float c, float d) { int w = __builtin_amdgcn_cvt_pk_fp8_f32(a, b, 0, false); w = __builtin_amdgcn_cvt_pk_fp8_f32(c, d, w, true); return (unsigned)w; }
;     __device__ __forceinline__ CvtDesc desc(int qq) const { return cvt_desc(*F, item_of(qq), qq & 1, h); }
;     __device__ __forceinline__ void flush() { if (fitem >= 0) { cvt_flush(cvt_desc(*F, fitem, 0, h), img, h, F->lane); fitem = -1; } }
; __device__ __forceinline__ void cvt_to_lds(const CvtBuf& b, const CvtDesc& d, LAS unsigned char* img, const LAS float* gl, int sub2, int h, int lane) {
;     const int hh = lane >> 5, l5 = lane & 31;
;     float gs[16];
;     const bool use_g = d.map == 2;
; #pragma unroll
;     for (int q = 0; q < 4; ++q) { const f32x4 gv = *(const LAS f32x4*)(gl + d.k0 + 16 * hh + 4 * q);
; #pragma unroll
;         for (int j = 0; j < 4; ++j) gs[4 * q + j] = use_g ? gv[j] : WSCALE; }
;     const int c8 = 4 * h + 2 * sub2 + hh;
; #pragma unroll
;     for (int j = 0; j < 4; ++j) { u32x4 o;
; #pragma unroll
;         for (int q = 0; q < 4; ++q) { const int i = 4 * q; o[q] = pk4_fp8(b.v[i][j] * gs[i], b.v[i + 1][j] * gs[i + 1], b.v[i + 2][j] * gs[i + 2], b.v[i + 3][j] * gs[i + 3]); }
;         *(LAS u32x4*)(img + (4 * l5 + j) * 128 + 16 * (c8 ^ (l5 & 7))) = o; }
; }
;     __device__ __forceinline__ void drain() {
;     ...
;         while (q < nq) {
;             if (q + 1 < nq) cvt_load(b2, desc(q + 1), F->lane);
;             cvt_to_lds(buf, desc(q), img, gl, q & 1, h, F->lane); if (q & 1) fitem = item_of(q); ++q;
;             if (fitem >= 0) { __syncthreads(); flush(); __syncthreads(); }
;             if (q >= nq) break;
;             if (q + 1 < nq) cvt_load(buf, desc(q + 1), F->lane);
;             cvt_to_lds(b2, desc(q), img, gl, q & 1, h, F->lane); if (q & 1) fitem = item_of(q); ++q;
;             if (fitem >= 0) { __syncthreads(); flush(); __syncthreads(); }
.LBB0_300:
	s_cmpk_lt_i32 s44, 0x4000
	s_cselect_b64 s[0:1], -1, 0
	s_and_b64 s[10:11], s[0:1], exec
	s_cselect_b32 s4, 5, 4
	s_lshr_b32 s4, s44, s4
	s_lshl_b32 s4, s4, 9
	s_and_b32 s4, s4, 0x1e00
	v_add_u32_e32 v136, s4, v139
	ds_read_b128 v[152:155], v136 offset:49152
	ds_read_b128 v[156:159], v136 offset:49168
	ds_read_b128 v[160:163], v136 offset:49184
	ds_read_b128 v[164:167], v136 offset:49200
	s_andn2_b64 vcc, exec, s[6:7]
	s_waitcnt lgkmcnt(3)
	v_cndmask_b32_e64 v132, v151, v152, s[0:1]
	v_cndmask_b32_e64 v137, v151, v153, s[0:1]
	v_cndmask_b32_e64 v168, v151, v154, s[0:1]
	s_waitcnt lgkmcnt(2)
	v_cndmask_b32_e64 v170, v151, v156, s[0:1]
	v_cndmask_b32_e64 v171, v151, v157, s[0:1]
	s_waitcnt vmcnt(31)
	v_mul_f32_e32 v153, v2, v132
	s_waitcnt vmcnt(30)
	v_mul_f32_e32 v154, v6, v137
	v_mov_b32_e32 v152, v133
	v_cvt_pk_fp8_f32 v152, v153, v154
	s_waitcnt vmcnt(27)
	v_mul_f32_e32 v154, v18, v170
	s_waitcnt vmcnt(26)
	v_mul_f32_e32 v157, v22, v171
	v_mov_b32_e32 v153, v133
	v_cvt_pk_fp8_f32 v153, v154, v157
	v_cndmask_b32_e64 v169, v151, v155, s[0:1]
	v_cndmask_b32_e64 v172, v151, v158, s[0:1]
	v_cndmask_b32_e64 v173, v151, v159, s[0:1]
	v_mul_f32_e32 v155, v10, v168
	v_mul_f32_e32 v156, v14, v169
	s_waitcnt lgkmcnt(1)
	v_cndmask_b32_e64 v174, v151, v160, s[0:1]
	v_cndmask_b32_e64 v175, v151, v161, s[0:1]
	v_cvt_pk_fp8_f32 v152, v155, v156 op_sel:[0,0,1]
	s_waitcnt vmcnt(25)
	v_mul_f32_e32 v154, v26, v172
	s_waitcnt vmcnt(24)
	v_mul_f32_e32 v155, v30, v173
	s_waitcnt lgkmcnt(0)
	v_cndmask_b32_e64 v178, v151, v164, s[0:1]
	v_cndmask_b32_e64 v179, v151, v165, s[0:1]
	v_cvt_pk_fp8_f32 v153, v154, v155 op_sel:[0,0,1]
	s_waitcnt vmcnt(23)
	v_mul_f32_e32 v155, v34, v174
	s_waitcnt vmcnt(22)
	v_mul_f32_e32 v156, v38, v175
	v_mov_b32_e32 v154, v133
	v_cvt_pk_fp8_f32 v154, v155, v156
	s_waitcnt vmcnt(19)
	v_mul_f32_e32 v156, v50, v178
	s_waitcnt vmcnt(18)
	v_mul_f32_e32 v159, v54, v179
	v_mov_b32_e32 v155, v133
	v_cvt_pk_fp8_f32 v155, v156, v159
	v_cndmask_b32_e64 v176, v151, v162, s[0:1]
	v_cndmask_b32_e64 v177, v151, v163, s[0:1]
	v_cndmask_b32_e64 v180, v151, v166, s[0:1]
	v_cndmask_b32_e64 v181, v151, v167, s[0:1]
	v_mul_f32_e32 v157, v42, v176
	v_mul_f32_e32 v158, v46, v177
	v_cvt_pk_fp8_f32 v154, v157, v158 op_sel:[0,0,1]
	s_waitcnt vmcnt(17)
	v_mul_f32_e32 v156, v58, v180
	s_waitcnt vmcnt(16)
	v_mul_f32_e32 v157, v62, v181
	v_cvt_pk_fp8_f32 v155, v156, v157 op_sel:[0,0,1]
	v_mul_f32_e32 v157, v3, v132
	v_mul_f32_e32 v158, v7, v137
	v_mov_b32_e32 v156, v133
	v_cvt_pk_fp8_f32 v156, v157, v158
	v_mul_f32_e32 v158, v19, v170
	v_mul_f32_e32 v161, v23, v171
	v_mov_b32_e32 v157, v133
	v_cvt_pk_fp8_f32 v157, v158, v161
	v_mul_f32_e32 v159, v11, v168
	v_mul_f32_e32 v160, v15, v169
	v_cvt_pk_fp8_f32 v156, v159, v160 op_sel:[0,0,1]
	v_mul_f32_e32 v158, v27, v172
	v_mul_f32_e32 v159, v31, v173
	v_cvt_pk_fp8_f32 v157, v158, v159 op_sel:[0,0,1]
	v_mul_f32_e32 v159, v35, v174
	v_mul_f32_e32 v160, v39, v175
	v_mov_b32_e32 v158, v133
	v_cvt_pk_fp8_f32 v158, v159, v160
	v_mul_f32_e32 v160, v51, v178
	v_mul_f32_e32 v163, v55, v179
	v_mov_b32_e32 v159, v133
	v_cvt_pk_fp8_f32 v159, v160, v163
	v_mul_f32_e32 v161, v43, v176
	v_mul_f32_e32 v162, v47, v177
	v_cvt_pk_fp8_f32 v158, v161, v162 op_sel:[0,0,1]
	v_mul_f32_e32 v160, v59, v180
	v_mul_f32_e32 v161, v63, v181
	v_cvt_pk_fp8_f32 v159, v160, v161 op_sel:[0,0,1]
	v_mul_f32_e32 v161, v4, v132
	v_mul_f32_e32 v162, v8, v137
	v_mov_b32_e32 v160, v133
	v_cvt_pk_fp8_f32 v160, v161, v162
	v_mul_f32_e32 v162, v20, v170
	v_mul_f32_e32 v165, v24, v171
	v_mov_b32_e32 v161, v133
	v_cvt_pk_fp8_f32 v161, v162, v165
	v_mul_f32_e32 v163, v12, v168
	v_mul_f32_e32 v164, v16, v169
	v_cvt_pk_fp8_f32 v160, v163, v164 op_sel:[0,0,1]
	v_mul_f32_e32 v162, v28, v172
	v_mul_f32_e32 v163, v32, v173
	v_cvt_pk_fp8_f32 v161, v162, v163 op_sel:[0,0,1]
	v_mul_f32_e32 v163, v36, v174
	v_mul_f32_e32 v164, v40, v175
	v_mov_b32_e32 v162, v133
	v_cvt_pk_fp8_f32 v162, v163, v164
	v_mul_f32_e32 v164, v52, v178
	v_mul_f32_e32 v167, v56, v179
	v_mov_b32_e32 v163, v133
	v_cvt_pk_fp8_f32 v163, v164, v167
	v_mul_f32_e32 v165, v44, v176
	v_mul_f32_e32 v166, v48, v177
	v_cvt_pk_fp8_f32 v162, v165, v166 op_sel:[0,0,1]
	v_mul_f32_e32 v164, v60, v180
	v_mul_f32_e32 v165, v64, v181
	v_cvt_pk_fp8_f32 v163, v164, v165 op_sel:[0,0,1]
	v_mul_f32_e32 v132, v5, v132
	v_mul_f32_e32 v137, v9, v137
	v_mov_b32_e32 v164, v133
	v_cvt_pk_fp8_f32 v164, v132, v137
	v_mul_f32_e32 v132, v21, v170
	v_mul_f32_e32 v137, v25, v171
	v_mov_b32_e32 v165, v133
	v_cvt_pk_fp8_f32 v165, v132, v137
	v_mul_f32_e32 v166, v13, v168
	v_mul_f32_e32 v167, v17, v169
	v_mul_f32_e32 v132, v29, v172
	v_mul_f32_e32 v137, v33, v173
	v_cvt_pk_fp8_f32 v164, v166, v167 op_sel:[0,0,1]
	v_cvt_pk_fp8_f32 v165, v132, v137 op_sel:[0,0,1]
	v_mul_f32_e32 v132, v37, v174
	v_mul_f32_e32 v137, v41, v175
	v_mov_b32_e32 v166, v133
	v_cvt_pk_fp8_f32 v166, v132, v137
	v_mul_f32_e32 v132, v53, v178
	v_mul_f32_e32 v137, v57, v179
	v_mov_b32_e32 v167, v133
	v_cvt_pk_fp8_f32 v167, v132, v137
	v_mul_f32_e32 v168, v45, v176
	v_mul_f32_e32 v169, v49, v177
	v_mul_f32_e32 v132, v61, v180
	v_mul_f32_e32 v137, v65, v181
	v_cvt_pk_fp8_f32 v166, v168, v169 op_sel:[0,0,1]
	v_cvt_pk_fp8_f32 v167, v132, v137 op_sel:[0,0,1]
	s_mov_b64 s[6:7], -1
	ds_write_b128 v149, v[152:155]
	ds_write_b128 v149, v[156:159] offset:128
	ds_write_b128 v149, v[160:163] offset:256
	ds_write_b128 v149, v[164:167] offset:384
	s_cbranch_vccnz .LBB0_293
	s_add_i32 s43, s43, 2
	s_cmp_ge_i32 s43, s34
	s_cselect_b64 s[6:7], -1, 0
	s_and_b64 vcc, exec, s[6:7]
	s_cbranch_vccz .Ldr1_goB
	s_waitcnt vmcnt(0)
	s_branch .LBB0_307
.Ldr1_goB:
	s_lshr_b32 s4, s43, 1
	s_mul_i32 s46, s4, 0xc0
	s_add_i32 s46, s46, s3
	s_cmpk_gt_i32 s46, 0x3fff
	s_mov_b64 s[36:37], -1
	s_cbranch_scc0 .LBB0_304
	s_add_i32 s4, s46, 0xffffc000
	s_lshr_b32 s4, s4, 8
	v_readlane_b32 s12, v254, 0
	s_lshr_b32 s45, s46, 4
	s_lshl_b64 s[10:11], s[4:5], 24
	v_readlane_b32 s14, v254, 2
	v_readlane_b32 s15, v254, 3
	s_add_u32 s10, s14, s10
	v_readlane_b32 s13, v254, 1
	v_readlane_b32 s16, v254, 4
	v_readlane_b32 s17, v254, 5
	v_readlane_b32 s18, v254, 6
	v_readlane_b32 s19, v254, 7
	s_addc_u32 s11, s15, s11
	s_mov_b64 s[36:37], 0

;     __device__ __forceinline__ CvtDesc desc(int qq) const { return cvt_desc(*F, item_of(qq), qq & 1, h); }
; __device__ __forceinline__ void cvt_load(CvtBuf& b, const CvtDesc& d, int lane) {
;     const float* p = d.W + (size_t)(d.k0 + 16 * (lane >> 5)) * d.ldw + d.n0 + 4 * (lane & 31);
; #pragma unroll
;     for (int i = 0; i < 16; ++i) b.v[i] = __builtin_nontemporal_load((const f32x4*)(p + (size_t)i * d.ldw));
; }
;     __device__ __forceinline__ void drain() {
;     ...
;             if (q + 1 < nq) cvt_load(buf, desc(q + 1), F->lane);
;             cvt_to_lds(b2, desc(q), img, gl, q & 1, h, F->lane); if (q & 1) fitem = item_of(q); ++q;
.LBB0_306:
	s_lshl_b32 s15, s45, 7
	s_and_b32 s15, s15, 0x780
	v_or_b32_e32 v2, s15, v131
	v_mul_u32_u24_e32 v2, s14, v2
	v_lshlrev_b32_e32 v132, 2, v2
	s_lshl_b32 s4, s4, 7
	v_lshl_add_u64 v[2:3], s[10:11], 0, v[132:133]
	v_lshl_add_u64 v[2:3], s[4:5], 2, v[2:3]
	v_lshlrev_b32_e32 v132, 2, v130
	v_lshl_add_u64 v[2:3], v[2:3], 0, v[132:133]
	s_lshl_b32 s4, s14, 2
	v_lshl_add_u64 v[10:11], v[2:3], 0, s[4:5]
	global_load_dwordx4 v[2:5], v[2:3], off nt
	s_nop 0
	global_load_dwordx4 v[6:9], v[10:11], off nt
	v_lshl_add_u64 v[10:11], v[10:11], 0, s[4:5]
	v_lshl_add_u64 v[18:19], v[10:11], 0, s[4:5]
	global_load_dwordx4 v[10:13], v[10:11], off nt
	s_nop 0
	global_load_dwordx4 v[14:17], v[18:19], off nt
	v_lshl_add_u64 v[18:19], v[18:19], 0, s[4:5]
	v_lshl_add_u64 v[26:27], v[18:19], 0, s[4:5]
	global_load_dwordx4 v[18:21], v[18:19], off nt
	s_nop 0
	global_load_dwordx4 v[22:25], v[26:27], off nt
	v_lshl_add_u64 v[26:27], v[26:27], 0, s[4:5]
	v_lshl_add_u64 v[34:35], v[26:27], 0, s[4:5]
	v_lshl_add_u64 v[38:39], v[34:35], 0, s[4:5]
	v_lshl_add_u64 v[42:43], v[38:39], 0, s[4:5]
	v_lshl_add_u64 v[46:47], v[42:43], 0, s[4:5]
	v_lshl_add_u64 v[50:51], v[46:47], 0, s[4:5]
	v_lshl_add_u64 v[54:55], v[50:51], 0, s[4:5]
	v_lshl_add_u64 v[58:59], v[54:55], 0, s[4:5]
	v_lshl_add_u64 v[62:63], v[58:59], 0, s[4:5]
	global_load_dwordx4 v[26:29], v[26:27], off nt
	s_nop 0
	global_load_dwordx4 v[30:33], v[34:35], off nt
	s_nop 0
	global_load_dwordx4 v[34:37], v[38:39], off nt
	s_nop 0
	global_load_dwordx4 v[38:41], v[42:43], off nt
	s_nop 0
	global_load_dwordx4 v[42:45], v[46:47], off nt
	s_nop 0
	global_load_dwordx4 v[46:49], v[50:51], off nt
	s_nop 0
	global_load_dwordx4 v[50:53], v[54:55], off nt
	s_nop 0
	global_load_dwordx4 v[54:57], v[58:59], off nt
	s_nop 0
	global_load_dwordx4 v[58:61], v[62:63], off nt
	v_lshl_add_u64 v[62:63], v[62:63], 0, s[4:5]
	global_load_dwordx4 v[62:65], v[62:63], off nt
	s_waitcnt vmcnt(16)

; #define LAS __attribute__((address_space(3)))
; __device__ __forceinline__ unsigned pk4_fp8(float a, float b, float c, float d) { int w = __builtin_amdgcn_cvt_pk_fp8_f32(a, b, 0, false); w = __builtin_amdgcn_cvt_pk_fp8_f32(c, d, w, true); return (unsigned)w; }
; __device__ __forceinline__ void cvt_load(CvtBuf& b, const CvtDesc& d, int lane) {
;     const float* p = d.W + (size_t)(d.k0 + 16 * (lane >> 5)) * d.ldw + d.n0 + 4 * (lane & 31);
; #pragma unroll
;     for (int i = 0; i < 16; ++i) b.v[i] = __builtin_nontemporal_load((const f32x4*)(p + (size_t)i * d.ldw));
; }
; __device__ __forceinline__ void cvt_to_lds(const CvtBuf& b, const CvtDesc& d, LAS unsigned char* img, const LAS float* gl, int sub2, int h, int lane) {
;     const int hh = lane >> 5, l5 = lane & 31;
;     float gs[16];
;     const bool use_g = d.map == 2;
; #pragma unroll
;     for (int q = 0; q < 4; ++q) { const f32x4 gv = *(const LAS f32x4*)(gl + d.k0 + 16 * hh + 4 * q);
; #pragma unroll
;         for (int j = 0; j < 4; ++j) gs[4 * q + j] = use_g ? gv[j] : WSCALE; }
;     const int c8 = 4 * h + 2 * sub2 + hh;
; #pragma unroll
;     for (int j = 0; j < 4; ++j) { u32x4 o;
; #pragma unroll
;         for (int q = 0; q < 4; ++q) { const int i = 4 * q; o[q] = pk4_fp8(b.v[i][j] * gs[i], b.v[i + 1][j] * gs[i + 1], b.v[i + 2][j] * gs[i + 2], b.v[i + 3][j] * gs[i + 3]); }
;         *(LAS u32x4*)(img + (4 * l5 + j) * 128 + 16 * (c8 ^ (l5 & 7))) = o; }
; }
.LBB0_1278:
	s_or_b32 s0, s59, 1
	s_cmp_lt_u32 s0, s12
	s_cselect_b64 s[4:5], -1, 0
	s_cmp_ge_u32 s0, s12
	s_cbranch_scc0 .Ldr9_goA
	s_waitcnt vmcnt(0)
	s_branch .LBB0_1280
.Ldr9_goA:
	s_lshr_b32 s0, s59, 1
	s_mul_i32 s0, s0, s11
	s_add_i32 s60, s0, s10
	s_add_i32 s0, s60, 0xffffc000
	v_readlane_b32 s64, v254, 0
	s_lshr_b32 s0, s0, 8
	v_readlane_b32 s66, v254, 2
	v_readlane_b32 s67, v254, 3
	s_lshl_b64 s[8:9], s[0:1], 24
	s_mov_b64 s[22:23], s[66:67]
	s_add_u32 s8, s22, s8
	s_addc_u32 s9, s23, s9
	s_lshl_b32 s0, s60, 3
	s_and_b32 s0, s0, 0x780
	v_or_b32_e32 v66, s0, v1
	v_lshlrev_b32_e32 v130, 13, v66
	s_lshl_b32 s0, s60, 9
	v_lshl_add_u64 v[66:67], s[8:9], 0, v[130:131]
	s_and_b32 s0, s0, 0x1e00
	v_lshl_add_u64 v[66:67], v[66:67], 0, s[0:1]
	v_lshlrev_b32_e32 v130, 2, v132
	v_lshl_add_u64 v[122:123], v[66:67], 0, v[130:131]
	v_add_co_u32_e32 v66, vcc, s45, v122
	v_readlane_b32 s65, v254, 1
	s_nop 0
	v_addc_co_u32_e32 v67, vcc, 0, v123, vcc
	v_add_co_u32_e32 v70, vcc, s46, v122
	v_readlane_b32 s68, v254, 4
	s_nop 0
	v_addc_co_u32_e32 v71, vcc, 0, v123, vcc
	v_add_co_u32_e32 v74, vcc, s47, v122
	global_load_dwordx4 v[66:69], v[66:67], off nt
	s_nop 0
	global_load_dwordx4 v[70:73], v[70:71], off nt
	v_addc_co_u32_e32 v75, vcc, 0, v123, vcc
	v_add_co_u32_e32 v78, vcc, s48, v122
	v_readlane_b32 s69, v254, 5
	s_nop 0
	v_addc_co_u32_e32 v79, vcc, 0, v123, vcc
	v_add_co_u32_e32 v82, vcc, s49, v122
	global_load_dwordx4 v[74:77], v[74:75], off nt
	s_nop 0
	global_load_dwordx4 v[78:81], v[78:79], off nt
	v_addc_co_u32_e32 v83, vcc, 0, v123, vcc
	v_add_co_u32_e32 v86, vcc, s50, v122
	v_readlane_b32 s70, v254, 6
	s_nop 0
	v_addc_co_u32_e32 v87, vcc, 0, v123, vcc
	v_add_co_u32_e32 v90, vcc, s51, v122
	global_load_dwordx4 v[82:85], v[82:83], off nt
	s_nop 0
	global_load_dwordx4 v[86:89], v[86:87], off nt
	v_addc_co_u32_e32 v91, vcc, 0, v123, vcc
	v_add_co_u32_e32 v94, vcc, s54, v122
	v_readlane_b32 s71, v254, 7
	s_nop 0
	v_addc_co_u32_e32 v95, vcc, 0, v123, vcc
	v_add_co_u32_e32 v98, vcc, s55, v122
	global_load_dwordx4 v[90:93], v[90:91], off nt
	s_nop 0
	global_load_dwordx4 v[94:97], v[94:95], off nt
	v_addc_co_u32_e32 v99, vcc, 0, v123, vcc
	v_add_co_u32_e32 v102, vcc, s56, v122
	s_nop 1
	v_addc_co_u32_e32 v103, vcc, 0, v123, vcc
	v_add_co_u32_e32 v106, vcc, s57, v122
	global_load_dwordx4 v[98:101], v[98:99], off nt
	s_nop 0
	global_load_dwordx4 v[102:105], v[102:103], off nt
	v_addc_co_u32_e32 v107, vcc, 0, v123, vcc
	v_add_co_u32_e32 v110, vcc, s58, v122
	s_nop 1
	v_addc_co_u32_e32 v111, vcc, 0, v123, vcc
	v_add_co_u32_e32 v114, vcc, 0x58000, v122
	global_load_dwordx4 v[106:109], v[106:107], off nt
	s_nop 0
	global_load_dwordx4 v[110:113], v[110:111], off nt
	v_addc_co_u32_e32 v115, vcc, 0, v123, vcc
	v_add_co_u32_e32 v118, vcc, 0x5a000, v122
	s_nop 1
	v_addc_co_u32_e32 v119, vcc, 0, v123, vcc
	v_add_co_u32_e32 v124, vcc, 0x5c000, v122
	global_load_dwordx4 v[114:117], v[114:115], off nt
	s_nop 0
	global_load_dwordx4 v[118:121], v[118:119], off nt
	v_addc_co_u32_e32 v125, vcc, 0, v123, vcc
	v_add_co_u32_e32 v126, vcc, 0x5e000, v122
	s_nop 1
	v_addc_co_u32_e32 v127, vcc, 0, v123, vcc
	global_load_dwordx4 v[122:125], v[124:125], off nt
	s_nop 0
	global_load_dwordx4 v[126:129], v[126:127], off nt
.LBB0_1280:
	s_waitcnt vmcnt(31)
	v_mul_f32_e32 v130, 0x42800000, v2
	s_waitcnt vmcnt(30)
	v_mul_f32_e32 v137, 0x42800000, v6
	v_mov_b32_e32 v136, 0
	v_cvt_pk_fp8_f32 v136, v130, v137
	s_waitcnt vmcnt(27)
	v_mul_f32_e32 v130, 0x42800000, v18
	s_waitcnt vmcnt(26)
	v_mul_f32_e32 v140, 0x42800000, v22
	v_mov_b32_e32 v137, 0
	v_cvt_pk_fp8_f32 v137, v130, v140
	v_mul_f32_e32 v138, 0x42800000, v10
	v_mul_f32_e32 v139, 0x42800000, v14
	v_cvt_pk_fp8_f32 v136, v138, v139 op_sel:[0,0,1]
	s_waitcnt vmcnt(25)
	v_mul_f32_e32 v130, 0x42800000, v26
	s_waitcnt vmcnt(24)
	v_mul_f32_e32 v138, 0x42800000, v30
	v_cvt_pk_fp8_f32 v137, v130, v138 op_sel:[0,0,1]
	s_waitcnt vmcnt(23)
	v_mul_f32_e32 v130, 0x42800000, v34
	s_waitcnt vmcnt(22)
	v_mul_f32_e32 v139, 0x42800000, v38
	v_mov_b32_e32 v138, 0
	v_cvt_pk_fp8_f32 v138, v130, v139
	s_waitcnt vmcnt(19)
	v_mul_f32_e32 v130, 0x42800000, v50
	s_waitcnt vmcnt(18)
	v_mul_f32_e32 v142, 0x42800000, v54
	v_mov_b32_e32 v139, 0
	v_cvt_pk_fp8_f32 v139, v130, v142
	v_mul_f32_e32 v140, 0x42800000, v42
	v_mul_f32_e32 v141, 0x42800000, v46
	v_cvt_pk_fp8_f32 v138, v140, v141 op_sel:[0,0,1]
	s_waitcnt vmcnt(17)
	v_mul_f32_e32 v130, 0x42800000, v58
	s_waitcnt vmcnt(16)
; #define LAS __attribute__((address_space(3)))
; __device__ __forceinline__ unsigned pk4_fp8(float a, float b, float c, float d) { int w = __builtin_amdgcn_cvt_pk_fp8_f32(a, b, 0, false); w = __builtin_amdgcn_cvt_pk_fp8_f32(c, d, w, true); return (unsigned)w; }
;     __device__ __forceinline__ CvtDesc desc(int qq) const { return cvt_desc(*F, item_of(qq), qq & 1, h); }
;     __device__ __forceinline__ void flush() { if (fitem >= 0) { cvt_flush(cvt_desc(*F, fitem, 0, h), img, h, F->lane); fitem = -1; } }
; __device__ __forceinline__ void cvt_to_lds(const CvtBuf& b, const CvtDesc& d, LAS unsigned char* img, const LAS float* gl, int sub2, int h, int lane) {
;     const int hh = lane >> 5, l5 = lane & 31;
;     float gs[16];
;     const bool use_g = d.map == 2;
; #pragma unroll
;     for (int q = 0; q < 4; ++q) { const f32x4 gv = *(const LAS f32x4*)(gl + d.k0 + 16 * hh + 4 * q);
; #pragma unroll
;         for (int j = 0; j < 4; ++j) gs[4 * q + j] = use_g ? gv[j] : WSCALE; }
;     const int c8 = 4 * h + 2 * sub2 + hh;
; #pragma unroll
;     for (int j = 0; j < 4; ++j) { u32x4 o;
; #pragma unroll
;         for (int q = 0; q < 4; ++q) { const int i = 4 * q; o[q] = pk4_fp8(b.v[i][j] * gs[i], b.v[i + 1][j] * gs[i + 1], b.v[i + 2][j] * gs[i + 2], b.v[i + 3][j] * gs[i + 3]); }
;         *(LAS u32x4*)(img + (4 * l5 + j) * 128 + 16 * (c8 ^ (l5 & 7))) = o; }
; }
;     __device__ __forceinline__ void drain() {
;     ...
;         while (q < nq) {
;             if (q + 1 < nq) cvt_load(b2, desc(q + 1), F->lane);
;             cvt_to_lds(buf, desc(q), img, gl, q & 1, h, F->lane); if (q & 1) fitem = item_of(q); ++q;
;             if (fitem >= 0) { __syncthreads(); flush(); __syncthreads(); }
;             if (q >= nq) break;
;             if (q + 1 < nq) cvt_load(buf, desc(q + 1), F->lane);
;             cvt_to_lds(b2, desc(q), img, gl, q & 1, h, F->lane); if (q & 1) fitem = item_of(q); ++q;
	v_mul_f32_e32 v140, 0x42800000, v62
	v_cvt_pk_fp8_f32 v139, v130, v140 op_sel:[0,0,1]
	v_mul_f32_e32 v130, 0x42800000, v3
	v_mul_f32_e32 v141, 0x42800000, v7
	v_mov_b32_e32 v140, 0
	v_cvt_pk_fp8_f32 v140, v130, v141
	v_mul_f32_e32 v130, 0x42800000, v19
	v_mul_f32_e32 v154, 0x42800000, v23
	v_mov_b32_e32 v141, 0
	v_cvt_pk_fp8_f32 v141, v130, v154
	v_mul_f32_e32 v142, 0x42800000, v11
	v_mul_f32_e32 v143, 0x42800000, v15
	v_cvt_pk_fp8_f32 v140, v142, v143 op_sel:[0,0,1]
	v_mul_f32_e32 v130, 0x42800000, v27
	v_mul_f32_e32 v142, 0x42800000, v31
	v_cvt_pk_fp8_f32 v141, v130, v142 op_sel:[0,0,1]
	v_mul_f32_e32 v130, 0x42800000, v35
	v_mul_f32_e32 v143, 0x42800000, v39
	v_mov_b32_e32 v142, 0
	v_cvt_pk_fp8_f32 v142, v130, v143
	v_mul_f32_e32 v130, 0x42800000, v51
	v_mul_f32_e32 v156, 0x42800000, v55
	v_mov_b32_e32 v143, 0
	v_cvt_pk_fp8_f32 v143, v130, v156
	v_mul_f32_e32 v154, 0x42800000, v43
	v_mul_f32_e32 v155, 0x42800000, v47
	v_cvt_pk_fp8_f32 v142, v154, v155 op_sel:[0,0,1]
	v_mul_f32_e32 v130, 0x42800000, v59
	v_mul_f32_e32 v154, 0x42800000, v63
	v_cvt_pk_fp8_f32 v143, v130, v154 op_sel:[0,0,1]
	v_mul_f32_e32 v130, 0x42800000, v4
	v_mul_f32_e32 v155, 0x42800000, v8
	v_mov_b32_e32 v154, 0
	v_cvt_pk_fp8_f32 v154, v130, v155
	v_mul_f32_e32 v130, 0x42800000, v20
	v_mul_f32_e32 v158, 0x42800000, v24
	v_mov_b32_e32 v155, 0
	v_cvt_pk_fp8_f32 v155, v130, v158
	v_mul_f32_e32 v156, 0x42800000, v12
	v_mul_f32_e32 v157, 0x42800000, v16
	v_cvt_pk_fp8_f32 v154, v156, v157 op_sel:[0,0,1]
	v_mul_f32_e32 v130, 0x42800000, v28
	v_mul_f32_e32 v156, 0x42800000, v32
	v_cvt_pk_fp8_f32 v155, v130, v156 op_sel:[0,0,1]
	v_mul_f32_e32 v130, 0x42800000, v36
	v_mul_f32_e32 v157, 0x42800000, v40
	v_mov_b32_e32 v156, 0
	v_cvt_pk_fp8_f32 v156, v130, v157
	v_mul_f32_e32 v130, 0x42800000, v52
	v_mul_f32_e32 v160, 0x42800000, v56
	v_mov_b32_e32 v157, 0
	v_cvt_pk_fp8_f32 v157, v130, v160
	v_mul_f32_e32 v158, 0x42800000, v44
	v_mul_f32_e32 v159, 0x42800000, v48
	v_cvt_pk_fp8_f32 v156, v158, v159 op_sel:[0,0,1]
	v_mul_f32_e32 v130, 0x42800000, v60
	v_mul_f32_e32 v158, 0x42800000, v64
	v_cvt_pk_fp8_f32 v157, v130, v158 op_sel:[0,0,1]
	v_mul_f32_e32 v130, 0x42800000, v5
	v_mul_f32_e32 v159, 0x42800000, v9
	v_mov_b32_e32 v158, 0
	v_cvt_pk_fp8_f32 v158, v130, v159
	v_mul_f32_e32 v130, 0x42800000, v21
	v_mul_f32_e32 v162, 0x42800000, v25
	v_mov_b32_e32 v159, 0
	v_cvt_pk_fp8_f32 v159, v130, v162
	v_mul_f32_e32 v160, 0x42800000, v13
	v_mul_f32_e32 v161, 0x42800000, v17
	v_cvt_pk_fp8_f32 v158, v160, v161 op_sel:[0,0,1]
	v_mul_f32_e32 v130, 0x42800000, v29
	v_mul_f32_e32 v160, 0x42800000, v33
	v_cvt_pk_fp8_f32 v159, v130, v160 op_sel:[0,0,1]
	v_mul_f32_e32 v130, 0x42800000, v37
	v_mul_f32_e32 v161, 0x42800000, v41
	v_mov_b32_e32 v160, 0
	v_cvt_pk_fp8_f32 v160, v130, v161
	v_mul_f32_e32 v130, 0x42800000, v53
	v_mul_f32_e32 v164, 0x42800000, v57
	v_mov_b32_e32 v161, 0
	v_cvt_pk_fp8_f32 v161, v130, v164
	v_mul_f32_e32 v162, 0x42800000, v45
	v_mul_f32_e32 v163, 0x42800000, v49
	v_cvt_pk_fp8_f32 v160, v162, v163 op_sel:[0,0,1]
	v_mul_f32_e32 v130, 0x42800000, v61
	v_mul_f32_e32 v162, 0x42800000, v65
	v_cvt_pk_fp8_f32 v161, v130, v162 op_sel:[0,0,1]
	s_andn2_b64 vcc, exec, s[4:5]
	s_mov_b64 s[4:5], -1
	ds_write_b128 v152, v[136:139]
	ds_write_b128 v152, v[140:143] offset:128
	ds_write_b128 v152, v[154:157] offset:256
	ds_write_b128 v152, v[158:161] offset:384
	s_cbranch_vccnz .LBB0_1277
	s_add_i32 s59, s59, 2
	s_cmp_ge_u32 s59, s12
	s_cselect_b64 s[4:5], -1, 0
	s_and_b64 vcc, exec, s[4:5]
	s_cbranch_vccz .Ldr9_goB
	s_waitcnt vmcnt(0)
	s_branch .LBB0_1283
.Ldr9_goB:
	s_lshr_b32 s0, s59, 1
	s_mul_i32 s0, s0, s11
	s_add_i32 s60, s0, s10
	s_add_i32 s0, s60, 0xffffc000
	v_readlane_b32 s64, v254, 0
	s_lshr_b32 s0, s0, 8
	v_readlane_b32 s66, v254, 2
	v_readlane_b32 s67, v254, 3
	s_lshl_b64 s[8:9], s[0:1], 24
	s_mov_b64 s[22:23], s[66:67]
	s_add_u32 s8, s22, s8
	s_addc_u32 s9, s23, s9
	s_lshl_b32 s0, s60, 3
	s_and_b32 s0, s0, 0x780
	v_or_b32_e32 v2, s0, v1
	v_lshlrev_b32_e32 v130, 13, v2
	s_lshl_b32 s0, s60, 9
	v_lshl_add_u64 v[2:3], s[8:9], 0, v[130:131]
	s_and_b32 s0, s0, 0x1e00
	v_lshl_add_u64 v[2:3], v[2:3], 0, s[0:1]
	v_lshlrev_b32_e32 v130, 2, v132
	v_lshl_add_u64 v[58:59], v[2:3], 0, v[130:131]
	v_add_co_u32_e32 v6, vcc, s15, v58
	v_readlane_b32 s65, v254, 1
	s_nop 0
	v_addc_co_u32_e32 v7, vcc, 0, v59, vcc
	v_add_co_u32_e32 v10, vcc, s16, v58
	global_load_dwordx4 v[2:5], v[58:59], off nt
	s_nop 0
	global_load_dwordx4 v[6:9], v[6:7], off nt
	v_addc_co_u32_e32 v11, vcc, 0, v59, vcc
	v_add_co_u32_e32 v14, vcc, s17, v58
	v_readlane_b32 s68, v254, 4
	s_nop 0
	v_addc_co_u32_e32 v15, vcc, 0, v59, vcc
	v_add_co_u32_e32 v18, vcc, s18, v58
	global_load_dwordx4 v[10:13], v[10:11], off nt
	s_nop 0
	global_load_dwordx4 v[14:17], v[14:15], off nt
	v_addc_co_u32_e32 v19, vcc, 0, v59, vcc
	v_add_co_u32_e32 v22, vcc, s19, v58
	v_readlane_b32 s69, v254, 5
	s_nop 0
	v_addc_co_u32_e32 v23, vcc, 0, v59, vcc
	v_add_co_u32_e32 v26, vcc, s20, v58
	global_load_dwordx4 v[18:21], v[18:19], off nt
	s_nop 0
	global_load_dwordx4 v[22:25], v[22:23], off nt
	v_addc_co_u32_e32 v27, vcc, 0, v59, vcc
	v_add_co_u32_e32 v30, vcc, s36, v58
	v_readlane_b32 s70, v254, 6
	s_nop 0
	v_addc_co_u32_e32 v31, vcc, 0, v59, vcc
	v_add_co_u32_e32 v34, vcc, s37, v58
	global_load_dwordx4 v[26:29], v[26:27], off nt
	s_nop 0
	global_load_dwordx4 v[30:33], v[30:31], off nt
	v_addc_co_u32_e32 v35, vcc, 0, v59, vcc
	v_add_co_u32_e32 v38, vcc, s38, v58
	v_readlane_b32 s71, v254, 7
	s_nop 0
	v_addc_co_u32_e32 v39, vcc, 0, v59, vcc
	v_add_co_u32_e32 v42, vcc, s39, v58
	global_load_dwordx4 v[34:37], v[34:35], off nt
	s_nop 0
	global_load_dwordx4 v[38:41], v[38:39], off nt
	v_addc_co_u32_e32 v43, vcc, 0, v59, vcc
	v_add_co_u32_e32 v46, vcc, s13, v58
	s_nop 1
	v_addc_co_u32_e32 v47, vcc, 0, v59, vcc
	v_add_co_u32_e32 v50, vcc, s40, v58
	global_load_dwordx4 v[42:45], v[42:43], off nt
	s_nop 0
	global_load_dwordx4 v[46:49], v[46:47], off nt
	v_addc_co_u32_e32 v51, vcc, 0, v59, vcc
	v_add_co_u32_e32 v54, vcc, 0x1a000, v58
	s_nop 1
	v_addc_co_u32_e32 v55, vcc, 0, v59, vcc
	v_add_co_u32_e32 v60, vcc, 0x1c000, v58
	global_load_dwordx4 v[50:53], v[50:51], off nt
	s_nop 0
	global_load_dwordx4 v[54:57], v[54:55], off nt
	v_addc_co_u32_e32 v61, vcc, 0, v59, vcc
	v_add_co_u32_e32 v62, vcc, 0x1e000, v58
	s_nop 1
	v_addc_co_u32_e32 v63, vcc, 0, v59, vcc
	global_load_dwordx4 v[58:61], v[60:61], off nt
	s_nop 0
	global_load_dwordx4 v[62:65], v[62:63], off nt
	s_waitcnt vmcnt(16)
